# v35: v32 + scan-wave helper-flag poll without s_sleep
# speedup vs baseline: 1.0030x; 1.0016x over previous
.Lsc_poll:
	v_mov_b32_e32 v66, s11
	ds_read_b128 v[66:69], v66
	s_waitcnt lgkmcnt(0)
	v_min_u32_e32 v66, v66, v67
	v_min3_u32 v66, v66, v68, v69
	v_cmp_lt_u32_e32 vcc, s10, v66
	s_cbranch_vccnz .LBB0_569
	s_add_i32 s18, s18, -1
	s_cmp_eq_u32 s18, 0
	s_cbranch_scc1 .LBB0_569
	s_branch .Lsc_poll
